# speedup vs baseline: 1.0076x; 1.0053x over previous
.Lou_loop:
	s_waitcnt lgkmcnt(0)
	v_mfma_f32_16x16x32_bf16 v[64:67], v[176:179], v[160:163], v[64:67]
	ds_read_b128 v[200:203], v11 offset:0
	v_mfma_f32_16x16x32_bf16 v[68:71], v[176:179], v[164:167], v[68:71]
	ds_read_b128 v[204:207], v11 offset:2048
	v_mfma_f32_16x16x32_bf16 v[72:75], v[176:179], v[168:171], v[72:75]
	ds_read_b128 v[208:211], v11 offset:4096
	v_mfma_f32_16x16x32_bf16 v[76:79], v[176:179], v[172:175], v[76:79]
	ds_read_b128 v[212:215], v11 offset:6144
	v_mfma_f32_16x16x32_bf16 v[80:83], v[180:183], v[160:163], v[80:83]
	ds_read_b128 v[216:219], v13 offset:0
	v_mfma_f32_16x16x32_bf16 v[84:87], v[180:183], v[164:167], v[84:87]
	ds_read_b128 v[220:223], v13 offset:2048
	v_mfma_f32_16x16x32_bf16 v[88:91], v[180:183], v[168:171], v[88:91]
	ds_read_b128 v[224:227], v13 offset:4096
	v_mfma_f32_16x16x32_bf16 v[92:95], v[180:183], v[172:175], v[92:95]
	ds_read_b128 v[228:231], v13 offset:6144
	v_mfma_f32_16x16x32_bf16 v[96:99], v[184:187], v[160:163], v[96:99]
	ds_read_b128 v[232:235], v13 offset:8192
	v_mfma_f32_16x16x32_bf16 v[100:103], v[184:187], v[164:167], v[100:103]
	ds_read_b128 v[236:239], v13 offset:10240
	v_mfma_f32_16x16x32_bf16 v[104:107], v[184:187], v[168:171], v[104:107]
	s_add_u32 m0, s20, 0x5000
	v_mfma_f32_16x16x32_bf16 v[108:111], v[184:187], v[172:175], v[108:111]
	global_load_lds_dwordx4 v3, s[18:19]
	v_mfma_f32_16x16x32_bf16 v[112:115], v[188:191], v[160:163], v[112:115]
	s_add_u32 m0, s20, 0x6000
	v_mfma_f32_16x16x32_bf16 v[116:119], v[188:191], v[164:167], v[116:119]
	global_load_lds_dwordx4 v4, s[18:19]
	v_mfma_f32_16x16x32_bf16 v[120:123], v[188:191], v[168:171], v[120:123]
	s_add_u32 m0, s20, 0x7000
	v_mfma_f32_16x16x32_bf16 v[124:127], v[188:191], v[172:175], v[124:127]
	global_load_lds_dwordx4 v5, s[18:19]
	v_mfma_f32_16x16x32_bf16 v[128:131], v[192:195], v[160:163], v[128:131]
	s_add_u32 m0, s20, 0x8000
	v_mfma_f32_16x16x32_bf16 v[132:135], v[192:195], v[164:167], v[132:135]
	global_load_lds_dwordx4 v6, s[18:19]
	v_mfma_f32_16x16x32_bf16 v[136:139], v[192:195], v[168:171], v[136:139]
	s_add_u32 m0, s20, 0x9000
	v_mfma_f32_16x16x32_bf16 v[140:143], v[192:195], v[172:175], v[140:143]
	global_load_lds_dwordx4 v7, s[18:19]
	v_mfma_f32_16x16x32_bf16 v[144:147], v[196:199], v[160:163], v[144:147]
	s_add_u32 s16, s16, 0x80
	s_addc_u32 s17, s17, 0
	s_add_u32 s18, s18, 0x80
	s_addc_u32 s19, s19, 0
	v_mfma_f32_16x16x32_bf16 v[148:151], v[196:199], v[164:167], v[148:151]
	s_add_u32 s20, s20, 0xa000
	s_sub_u32 s22, s20, 0x28000
	s_cmp_ge_u32 s20, 0x28000
	s_cselect_b32 s20, s22, s20
	v_mfma_f32_16x16x32_bf16 v[152:155], v[196:199], v[168:171], v[152:155]
	v_add_u32_e32 v10, s21, v8
	v_add_u32_e32 v12, s21, v9
	v_xor_b32_e32 v11, 64, v10
	v_xor_b32_e32 v13, 64, v12
	v_mfma_f32_16x16x32_bf16 v[156:159], v[196:199], v[172:175], v[156:159]
	s_add_u32 s21, s21, 0xa000
	s_sub_u32 s23, s21, 0x28000
	s_cmp_ge_u32 s21, 0x28000
	s_cselect_b32 s21, s23, s21
	s_waitcnt lgkmcnt(0)
	v_mfma_f32_16x16x32_bf16 v[64:67], v[216:219], v[200:203], v[64:67]
	v_mfma_f32_16x16x32_bf16 v[68:71], v[216:219], v[204:207], v[68:71]
	v_mfma_f32_16x16x32_bf16 v[72:75], v[216:219], v[208:211], v[72:75]
	v_mfma_f32_16x16x32_bf16 v[76:79], v[216:219], v[212:215], v[76:79]
	s_waitcnt vmcnt(20)
	s_barrier
	v_mfma_f32_16x16x32_bf16 v[80:83], v[220:223], v[200:203], v[80:83]
	ds_read_b128 v[160:163], v10 offset:0
	v_mfma_f32_16x16x32_bf16 v[84:87], v[220:223], v[204:207], v[84:87]
	ds_read_b128 v[164:167], v10 offset:2048
	v_mfma_f32_16x16x32_bf16 v[88:91], v[220:223], v[208:211], v[88:91]
	ds_read_b128 v[168:171], v10 offset:4096
	v_mfma_f32_16x16x32_bf16 v[92:95], v[220:223], v[212:215], v[92:95]
	ds_read_b128 v[172:175], v10 offset:6144
	v_mfma_f32_16x16x32_bf16 v[96:99], v[224:227], v[200:203], v[96:99]
	ds_read_b128 v[176:179], v12 offset:0
	v_mfma_f32_16x16x32_bf16 v[100:103], v[224:227], v[204:207], v[100:103]
	ds_read_b128 v[180:183], v12 offset:2048
	v_mfma_f32_16x16x32_bf16 v[104:107], v[224:227], v[208:211], v[104:107]
	ds_read_b128 v[184:187], v12 offset:4096
	v_mfma_f32_16x16x32_bf16 v[108:111], v[224:227], v[212:215], v[108:111]
	ds_read_b128 v[188:191], v12 offset:6144
	v_mfma_f32_16x16x32_bf16 v[112:115], v[228:231], v[200:203], v[112:115]
	ds_read_b128 v[192:195], v12 offset:8192
	v_mfma_f32_16x16x32_bf16 v[116:119], v[228:231], v[204:207], v[116:119]
	ds_read_b128 v[196:199], v12 offset:10240
	v_mfma_f32_16x16x32_bf16 v[120:123], v[228:231], v[208:211], v[120:123]
	s_add_u32 m0, s20, 0x0
	v_mfma_f32_16x16x32_bf16 v[124:127], v[228:231], v[212:215], v[124:127]
	global_load_lds_dwordx4 v2, s[16:17]
	v_mfma_f32_16x16x32_bf16 v[128:131], v[232:235], v[200:203], v[128:131]
	s_add_u32 m0, s20, 0x1000
	v_mfma_f32_16x16x32_bf16 v[132:135], v[232:235], v[204:207], v[132:135]
	global_load_lds_dwordx4 v3, s[16:17]
	v_mfma_f32_16x16x32_bf16 v[136:139], v[232:235], v[208:211], v[136:139]
	s_add_u32 m0, s20, 0x2000
	v_mfma_f32_16x16x32_bf16 v[140:143], v[232:235], v[212:215], v[140:143]
	global_load_lds_dwordx4 v4, s[16:17]
	v_mfma_f32_16x16x32_bf16 v[144:147], v[236:239], v[200:203], v[144:147]
	s_add_u32 m0, s20, 0x3000
	v_mfma_f32_16x16x32_bf16 v[148:151], v[236:239], v[204:207], v[148:151]
	global_load_lds_dwordx4 v5, s[16:17]
	v_mfma_f32_16x16x32_bf16 v[152:155], v[236:239], v[208:211], v[152:155]
	s_add_u32 m0, s20, 0x4000
	v_mfma_f32_16x16x32_bf16 v[156:159], v[236:239], v[212:215], v[156:159]
	global_load_lds_dwordx4 v2, s[18:19]
	s_add_u32 s15, s15, 1
	s_cmp_lt_u32 s15, 8
	s_cbranch_scc1 .Lou_loop
	s_waitcnt lgkmcnt(0)
	v_mfma_f32_16x16x32_bf16 v[64:67], v[176:179], v[160:163], v[64:67]
	ds_read_b128 v[200:203], v11 offset:0
	v_mfma_f32_16x16x32_bf16 v[68:71], v[176:179], v[164:167], v[68:71]
	ds_read_b128 v[204:207], v11 offset:2048
	v_mfma_f32_16x16x32_bf16 v[72:75], v[176:179], v[168:171], v[72:75]
	ds_read_b128 v[208:211], v11 offset:4096
	v_mfma_f32_16x16x32_bf16 v[76:79], v[176:179], v[172:175], v[76:79]
	ds_read_b128 v[212:215], v11 offset:6144
	v_mfma_f32_16x16x32_bf16 v[80:83], v[180:183], v[160:163], v[80:83]
	ds_read_b128 v[216:219], v13 offset:0
	v_mfma_f32_16x16x32_bf16 v[84:87], v[180:183], v[164:167], v[84:87]
	ds_read_b128 v[220:223], v13 offset:2048
	v_mfma_f32_16x16x32_bf16 v[88:91], v[180:183], v[168:171], v[88:91]
	ds_read_b128 v[224:227], v13 offset:4096
	v_mfma_f32_16x16x32_bf16 v[92:95], v[180:183], v[172:175], v[92:95]
	ds_read_b128 v[228:231], v13 offset:6144
	v_mfma_f32_16x16x32_bf16 v[96:99], v[184:187], v[160:163], v[96:99]
	ds_read_b128 v[232:235], v13 offset:8192
	v_mfma_f32_16x16x32_bf16 v[100:103], v[184:187], v[164:167], v[100:103]
	ds_read_b128 v[236:239], v13 offset:10240
	v_mfma_f32_16x16x32_bf16 v[104:107], v[184:187], v[168:171], v[104:107]
	s_add_u32 m0, s20, 0x5000
	v_mfma_f32_16x16x32_bf16 v[108:111], v[184:187], v[172:175], v[108:111]
	global_load_lds_dwordx4 v3, s[18:19]
	v_mfma_f32_16x16x32_bf16 v[112:115], v[188:191], v[160:163], v[112:115]
	s_add_u32 m0, s20, 0x6000
	v_mfma_f32_16x16x32_bf16 v[116:119], v[188:191], v[164:167], v[116:119]
	global_load_lds_dwordx4 v4, s[18:19]
	v_mfma_f32_16x16x32_bf16 v[120:123], v[188:191], v[168:171], v[120:123]
	s_add_u32 m0, s20, 0x7000
	v_mfma_f32_16x16x32_bf16 v[124:127], v[188:191], v[172:175], v[124:127]
	global_load_lds_dwordx4 v5, s[18:19]
	v_mfma_f32_16x16x32_bf16 v[128:131], v[192:195], v[160:163], v[128:131]
	s_add_u32 m0, s20, 0x8000
	v_mfma_f32_16x16x32_bf16 v[132:135], v[192:195], v[164:167], v[132:135]
	global_load_lds_dwordx4 v6, s[18:19]
	v_mfma_f32_16x16x32_bf16 v[136:139], v[192:195], v[168:171], v[136:139]
	s_add_u32 m0, s20, 0x9000
	v_mfma_f32_16x16x32_bf16 v[140:143], v[192:195], v[172:175], v[140:143]
	global_load_lds_dwordx4 v7, s[18:19]
	v_mfma_f32_16x16x32_bf16 v[144:147], v[196:199], v[160:163], v[144:147]
	s_add_u32 s16, s16, 0x80
	s_addc_u32 s17, s17, 0
	s_add_u32 s18, s18, 0x80
	s_addc_u32 s19, s19, 0
	v_mfma_f32_16x16x32_bf16 v[148:151], v[196:199], v[164:167], v[148:151]
	s_add_u32 s20, s20, 0xa000
	s_sub_u32 s22, s20, 0x28000
	s_cmp_ge_u32 s20, 0x28000
	s_cselect_b32 s20, s22, s20
	v_mfma_f32_16x16x32_bf16 v[152:155], v[196:199], v[168:171], v[152:155]
	v_add_u32_e32 v10, s21, v8
	v_add_u32_e32 v12, s21, v9
	v_xor_b32_e32 v11, 64, v10
	v_xor_b32_e32 v13, 64, v12
	v_mfma_f32_16x16x32_bf16 v[156:159], v[196:199], v[172:175], v[156:159]
	s_add_u32 s21, s21, 0xa000
	s_sub_u32 s23, s21, 0x28000
	s_cmp_ge_u32 s21, 0x28000
	s_cselect_b32 s21, s23, s21
	s_waitcnt lgkmcnt(0)
	v_mfma_f32_16x16x32_bf16 v[64:67], v[216:219], v[200:203], v[64:67]
	v_mfma_f32_16x16x32_bf16 v[68:71], v[216:219], v[204:207], v[68:71]
	v_mfma_f32_16x16x32_bf16 v[72:75], v[216:219], v[208:211], v[72:75]
	v_mfma_f32_16x16x32_bf16 v[76:79], v[216:219], v[212:215], v[76:79]
	s_waitcnt vmcnt(20)
	s_barrier
	v_mfma_f32_16x16x32_bf16 v[80:83], v[220:223], v[200:203], v[80:83]
	ds_read_b128 v[160:163], v10 offset:0
	v_mfma_f32_16x16x32_bf16 v[84:87], v[220:223], v[204:207], v[84:87]
	ds_read_b128 v[164:167], v10 offset:2048
	v_mfma_f32_16x16x32_bf16 v[88:91], v[220:223], v[208:211], v[88:91]
	ds_read_b128 v[168:171], v10 offset:4096
	v_mfma_f32_16x16x32_bf16 v[92:95], v[220:223], v[212:215], v[92:95]
	ds_read_b128 v[172:175], v10 offset:6144
	v_mfma_f32_16x16x32_bf16 v[96:99], v[224:227], v[200:203], v[96:99]
	ds_read_b128 v[176:179], v12 offset:0
	v_mfma_f32_16x16x32_bf16 v[100:103], v[224:227], v[204:207], v[100:103]
	ds_read_b128 v[180:183], v12 offset:2048
	v_mfma_f32_16x16x32_bf16 v[104:107], v[224:227], v[208:211], v[104:107]
	ds_read_b128 v[184:187], v12 offset:4096
	v_mfma_f32_16x16x32_bf16 v[108:111], v[224:227], v[212:215], v[108:111]
	ds_read_b128 v[188:191], v12 offset:6144
	v_mfma_f32_16x16x32_bf16 v[112:115], v[228:231], v[200:203], v[112:115]
	ds_read_b128 v[192:195], v12 offset:8192
	v_mfma_f32_16x16x32_bf16 v[116:119], v[228:231], v[204:207], v[116:119]
	ds_read_b128 v[196:199], v12 offset:10240
	v_mfma_f32_16x16x32_bf16 v[120:123], v[228:231], v[208:211], v[120:123]
	global_load_dwordx4 v[240:243], v60, s[24:25]
	v_mfma_f32_16x16x32_bf16 v[124:127], v[228:231], v[212:215], v[124:127]
	global_load_dwordx4 v[244:247], v60, s[24:25] offset:64
	v_mfma_f32_16x16x32_bf16 v[128:131], v[232:235], v[200:203], v[128:131]
	global_load_dwordx4 v[248:251], v60, s[24:25] offset:128
	v_mfma_f32_16x16x32_bf16 v[132:135], v[232:235], v[204:207], v[132:135]
	global_load_dwordx4 v[252:255], v60, s[24:25] offset:192
	v_mfma_f32_16x16x32_bf16 v[136:139], v[232:235], v[208:211], v[136:139]
	global_load_dwordx4 v[48:51], v60, s[24:25] offset:256
	v_mfma_f32_16x16x32_bf16 v[140:143], v[232:235], v[212:215], v[140:143]
	global_load_dwordx4 v[52:55], v60, s[24:25] offset:320
	v_mfma_f32_16x16x32_bf16 v[144:147], v[236:239], v[200:203], v[144:147]
	global_load_dwordx4 v[16:19], v56, s[8:9] offset:0
	v_mfma_f32_16x16x32_bf16 v[148:151], v[236:239], v[204:207], v[148:151]
	global_load_dwordx4 v[20:23], v56, s[8:9] offset:64
	v_mfma_f32_16x16x32_bf16 v[152:155], v[236:239], v[208:211], v[152:155]
	global_load_dwordx4 v[24:27], v56, s[8:9] offset:128
	v_mfma_f32_16x16x32_bf16 v[156:159], v[236:239], v[212:215], v[156:159]
	global_load_dwordx4 v[28:31], v56, s[8:9] offset:192
	global_load_dwordx4 v[32:35], v56, s[8:9] offset:256
	global_load_dwordx4 v[36:39], v56, s[8:9] offset:320
	global_load_dwordx4 v[40:43], v57, s[8:9] offset:0
	global_load_dwordx4 v[44:47], v57, s[8:9] offset:64
	s_waitcnt lgkmcnt(0)
	v_mfma_f32_16x16x32_bf16 v[64:67], v[176:179], v[160:163], v[64:67]
	ds_read_b128 v[200:203], v11 offset:0
	v_mfma_f32_16x16x32_bf16 v[68:71], v[176:179], v[164:167], v[68:71]
	ds_read_b128 v[204:207], v11 offset:2048
	v_mfma_f32_16x16x32_bf16 v[72:75], v[176:179], v[168:171], v[72:75]
	ds_read_b128 v[208:211], v11 offset:4096
	v_mfma_f32_16x16x32_bf16 v[76:79], v[176:179], v[172:175], v[76:79]
	ds_read_b128 v[212:215], v11 offset:6144
	v_mfma_f32_16x16x32_bf16 v[80:83], v[180:183], v[160:163], v[80:83]
	ds_read_b128 v[216:219], v13 offset:0
	v_mfma_f32_16x16x32_bf16 v[84:87], v[180:183], v[164:167], v[84:87]
	ds_read_b128 v[220:223], v13 offset:2048
	v_mfma_f32_16x16x32_bf16 v[88:91], v[180:183], v[168:171], v[88:91]
	ds_read_b128 v[224:227], v13 offset:4096
	v_mfma_f32_16x16x32_bf16 v[92:95], v[180:183], v[172:175], v[92:95]
	ds_read_b128 v[228:231], v13 offset:6144
	v_mfma_f32_16x16x32_bf16 v[96:99], v[184:187], v[160:163], v[96:99]
	ds_read_b128 v[232:235], v13 offset:8192
	v_mfma_f32_16x16x32_bf16 v[100:103], v[184:187], v[164:167], v[100:103]
	ds_read_b128 v[236:239], v13 offset:10240
	v_mfma_f32_16x16x32_bf16 v[104:107], v[184:187], v[168:171], v[104:107]
	v_mfma_f32_16x16x32_bf16 v[108:111], v[184:187], v[172:175], v[108:111]
	v_mfma_f32_16x16x32_bf16 v[112:115], v[188:191], v[160:163], v[112:115]
	v_mfma_f32_16x16x32_bf16 v[116:119], v[188:191], v[164:167], v[116:119]
	v_mfma_f32_16x16x32_bf16 v[120:123], v[188:191], v[168:171], v[120:123]
	v_mfma_f32_16x16x32_bf16 v[124:127], v[188:191], v[172:175], v[124:127]
	v_mfma_f32_16x16x32_bf16 v[128:131], v[192:195], v[160:163], v[128:131]
	v_mfma_f32_16x16x32_bf16 v[132:135], v[192:195], v[164:167], v[132:135]
	v_mfma_f32_16x16x32_bf16 v[136:139], v[192:195], v[168:171], v[136:139]
	v_mfma_f32_16x16x32_bf16 v[140:143], v[192:195], v[172:175], v[140:143]
	v_mfma_f32_16x16x32_bf16 v[144:147], v[196:199], v[160:163], v[144:147]
	v_add_u32_e32 v10, s21, v8
	v_add_u32_e32 v12, s21, v9
	v_xor_b32_e32 v11, 64, v10
	v_xor_b32_e32 v13, 64, v12
	v_mfma_f32_16x16x32_bf16 v[148:151], v[196:199], v[164:167], v[148:151]
	s_add_u32 s21, s21, 0xa000
	s_sub_u32 s23, s21, 0x28000
	s_cmp_ge_u32 s21, 0x28000
	s_cselect_b32 s21, s23, s21
	v_mfma_f32_16x16x32_bf16 v[152:155], v[196:199], v[168:171], v[152:155]
	v_mfma_f32_16x16x32_bf16 v[156:159], v[196:199], v[172:175], v[156:159]
	s_waitcnt lgkmcnt(0)
	v_mfma_f32_16x16x32_bf16 v[64:67], v[216:219], v[200:203], v[64:67]
	v_mfma_f32_16x16x32_bf16 v[68:71], v[216:219], v[204:207], v[68:71]
	v_mfma_f32_16x16x32_bf16 v[72:75], v[216:219], v[208:211], v[72:75]
	v_mfma_f32_16x16x32_bf16 v[76:79], v[216:219], v[212:215], v[76:79]
	s_waitcnt vmcnt(24)
	s_barrier
	v_mfma_f32_16x16x32_bf16 v[80:83], v[220:223], v[200:203], v[80:83]
	ds_read_b128 v[160:163], v10 offset:0
	v_mfma_f32_16x16x32_bf16 v[84:87], v[220:223], v[204:207], v[84:87]
	ds_read_b128 v[164:167], v10 offset:2048
	v_mfma_f32_16x16x32_bf16 v[88:91], v[220:223], v[208:211], v[88:91]
	ds_read_b128 v[168:171], v10 offset:4096
	v_mfma_f32_16x16x32_bf16 v[92:95], v[220:223], v[212:215], v[92:95]
	ds_read_b128 v[172:175], v10 offset:6144
	v_mfma_f32_16x16x32_bf16 v[96:99], v[224:227], v[200:203], v[96:99]
	ds_read_b128 v[176:179], v12 offset:0
	v_mfma_f32_16x16x32_bf16 v[100:103], v[224:227], v[204:207], v[100:103]
	ds_read_b128 v[180:183], v12 offset:2048
	v_mfma_f32_16x16x32_bf16 v[104:107], v[224:227], v[208:211], v[104:107]
	ds_read_b128 v[184:187], v12 offset:4096
	v_mfma_f32_16x16x32_bf16 v[108:111], v[224:227], v[212:215], v[108:111]
	ds_read_b128 v[188:191], v12 offset:6144
	v_mfma_f32_16x16x32_bf16 v[112:115], v[228:231], v[200:203], v[112:115]
	ds_read_b128 v[192:195], v12 offset:8192
	v_mfma_f32_16x16x32_bf16 v[116:119], v[228:231], v[204:207], v[116:119]
	ds_read_b128 v[196:199], v12 offset:10240
	v_mfma_f32_16x16x32_bf16 v[120:123], v[228:231], v[208:211], v[120:123]
	v_mfma_f32_16x16x32_bf16 v[124:127], v[228:231], v[212:215], v[124:127]
	v_mfma_f32_16x16x32_bf16 v[128:131], v[232:235], v[200:203], v[128:131]
	v_mfma_f32_16x16x32_bf16 v[132:135], v[232:235], v[204:207], v[132:135]
	v_mfma_f32_16x16x32_bf16 v[136:139], v[232:235], v[208:211], v[136:139]
	v_mfma_f32_16x16x32_bf16 v[140:143], v[232:235], v[212:215], v[140:143]
	v_mfma_f32_16x16x32_bf16 v[144:147], v[236:239], v[200:203], v[144:147]
	v_mfma_f32_16x16x32_bf16 v[148:151], v[236:239], v[204:207], v[148:151]
	v_mfma_f32_16x16x32_bf16 v[152:155], v[236:239], v[208:211], v[152:155]
	v_mfma_f32_16x16x32_bf16 v[156:159], v[236:239], v[212:215], v[156:159]
	s_waitcnt lgkmcnt(0)
	v_mfma_f32_16x16x32_bf16 v[64:67], v[176:179], v[160:163], v[64:67]
	ds_read_b128 v[200:203], v11 offset:0
	v_mfma_f32_16x16x32_bf16 v[68:71], v[176:179], v[164:167], v[68:71]
	ds_read_b128 v[204:207], v11 offset:2048
	v_mfma_f32_16x16x32_bf16 v[72:75], v[176:179], v[168:171], v[72:75]
	ds_read_b128 v[208:211], v11 offset:4096
	v_mfma_f32_16x16x32_bf16 v[76:79], v[176:179], v[172:175], v[76:79]
	ds_read_b128 v[212:215], v11 offset:6144
	v_mfma_f32_16x16x32_bf16 v[80:83], v[180:183], v[160:163], v[80:83]
	ds_read_b128 v[216:219], v13 offset:0
	v_mfma_f32_16x16x32_bf16 v[84:87], v[180:183], v[164:167], v[84:87]
	ds_read_b128 v[220:223], v13 offset:2048
	v_mfma_f32_16x16x32_bf16 v[88:91], v[180:183], v[168:171], v[88:91]
	ds_read_b128 v[224:227], v13 offset:4096
	v_mfma_f32_16x16x32_bf16 v[92:95], v[180:183], v[172:175], v[92:95]
	ds_read_b128 v[228:231], v13 offset:6144
	v_mfma_f32_16x16x32_bf16 v[96:99], v[184:187], v[160:163], v[96:99]
	ds_read_b128 v[232:235], v13 offset:8192
	v_mfma_f32_16x16x32_bf16 v[100:103], v[184:187], v[164:167], v[100:103]
	ds_read_b128 v[236:239], v13 offset:10240
	v_mfma_f32_16x16x32_bf16 v[104:107], v[184:187], v[168:171], v[104:107]
	v_mfma_f32_16x16x32_bf16 v[108:111], v[184:187], v[172:175], v[108:111]
	v_mfma_f32_16x16x32_bf16 v[112:115], v[188:191], v[160:163], v[112:115]
	v_mfma_f32_16x16x32_bf16 v[116:119], v[188:191], v[164:167], v[116:119]
	v_mfma_f32_16x16x32_bf16 v[120:123], v[188:191], v[168:171], v[120:123]
	v_mfma_f32_16x16x32_bf16 v[124:127], v[188:191], v[172:175], v[124:127]
	v_mfma_f32_16x16x32_bf16 v[128:131], v[192:195], v[160:163], v[128:131]
	v_mfma_f32_16x16x32_bf16 v[132:135], v[192:195], v[164:167], v[132:135]
	v_mfma_f32_16x16x32_bf16 v[136:139], v[192:195], v[168:171], v[136:139]
	v_mfma_f32_16x16x32_bf16 v[140:143], v[192:195], v[172:175], v[140:143]
	v_mfma_f32_16x16x32_bf16 v[144:147], v[196:199], v[160:163], v[144:147]
	v_add_u32_e32 v10, s21, v8
	v_add_u32_e32 v12, s21, v9
	v_xor_b32_e32 v11, 64, v10
	v_xor_b32_e32 v13, 64, v12
	v_mfma_f32_16x16x32_bf16 v[148:151], v[196:199], v[164:167], v[148:151]
	s_add_u32 s21, s21, 0xa000
	s_sub_u32 s23, s21, 0x28000
	s_cmp_ge_u32 s21, 0x28000
	s_cselect_b32 s21, s23, s21
	v_mfma_f32_16x16x32_bf16 v[152:155], v[196:199], v[168:171], v[152:155]
	v_mfma_f32_16x16x32_bf16 v[156:159], v[196:199], v[172:175], v[156:159]
	s_waitcnt lgkmcnt(0)
	v_mfma_f32_16x16x32_bf16 v[64:67], v[216:219], v[200:203], v[64:67]
	v_mfma_f32_16x16x32_bf16 v[68:71], v[216:219], v[204:207], v[68:71]
	v_mfma_f32_16x16x32_bf16 v[72:75], v[216:219], v[208:211], v[72:75]
	v_mfma_f32_16x16x32_bf16 v[76:79], v[216:219], v[212:215], v[76:79]
	s_waitcnt vmcnt(14)
	s_barrier
	v_mfma_f32_16x16x32_bf16 v[80:83], v[220:223], v[200:203], v[80:83]
	ds_read_b128 v[160:163], v10 offset:0
	v_mfma_f32_16x16x32_bf16 v[84:87], v[220:223], v[204:207], v[84:87]
	ds_read_b128 v[164:167], v10 offset:2048
	v_mfma_f32_16x16x32_bf16 v[88:91], v[220:223], v[208:211], v[88:91]
	ds_read_b128 v[168:171], v10 offset:4096
	v_mfma_f32_16x16x32_bf16 v[92:95], v[220:223], v[212:215], v[92:95]
	ds_read_b128 v[172:175], v10 offset:6144
	v_mfma_f32_16x16x32_bf16 v[96:99], v[224:227], v[200:203], v[96:99]
	ds_read_b128 v[176:179], v12 offset:0
	v_mfma_f32_16x16x32_bf16 v[100:103], v[224:227], v[204:207], v[100:103]
	ds_read_b128 v[180:183], v12 offset:2048
	v_mfma_f32_16x16x32_bf16 v[104:107], v[224:227], v[208:211], v[104:107]
	ds_read_b128 v[184:187], v12 offset:4096
	v_mfma_f32_16x16x32_bf16 v[108:111], v[224:227], v[212:215], v[108:111]
	ds_read_b128 v[188:191], v12 offset:6144
	v_mfma_f32_16x16x32_bf16 v[112:115], v[228:231], v[200:203], v[112:115]
	ds_read_b128 v[192:195], v12 offset:8192
	v_mfma_f32_16x16x32_bf16 v[116:119], v[228:231], v[204:207], v[116:119]
	ds_read_b128 v[196:199], v12 offset:10240
	v_mfma_f32_16x16x32_bf16 v[120:123], v[228:231], v[208:211], v[120:123]
	v_mfma_f32_16x16x32_bf16 v[124:127], v[228:231], v[212:215], v[124:127]
	v_mfma_f32_16x16x32_bf16 v[128:131], v[232:235], v[200:203], v[128:131]
	v_mfma_f32_16x16x32_bf16 v[132:135], v[232:235], v[204:207], v[132:135]
	v_mfma_f32_16x16x32_bf16 v[136:139], v[232:235], v[208:211], v[136:139]
	v_mfma_f32_16x16x32_bf16 v[140:143], v[232:235], v[212:215], v[140:143]
	v_mfma_f32_16x16x32_bf16 v[144:147], v[236:239], v[200:203], v[144:147]
	v_mfma_f32_16x16x32_bf16 v[148:151], v[236:239], v[204:207], v[148:151]
	v_mfma_f32_16x16x32_bf16 v[152:155], v[236:239], v[208:211], v[152:155]
	v_mfma_f32_16x16x32_bf16 v[156:159], v[236:239], v[212:215], v[156:159]
	s_waitcnt lgkmcnt(0)
	v_mfma_f32_16x16x32_bf16 v[64:67], v[176:179], v[160:163], v[64:67]
	ds_read_b128 v[200:203], v11 offset:0
	v_mfma_f32_16x16x32_bf16 v[68:71], v[176:179], v[164:167], v[68:71]
	ds_read_b128 v[204:207], v11 offset:2048
	v_mfma_f32_16x16x32_bf16 v[72:75], v[176:179], v[168:171], v[72:75]
	ds_read_b128 v[208:211], v11 offset:4096
	v_mfma_f32_16x16x32_bf16 v[76:79], v[176:179], v[172:175], v[76:79]
	ds_read_b128 v[212:215], v11 offset:6144
	v_mfma_f32_16x16x32_bf16 v[80:83], v[180:183], v[160:163], v[80:83]
	ds_read_b128 v[216:219], v13 offset:0
	v_mfma_f32_16x16x32_bf16 v[84:87], v[180:183], v[164:167], v[84:87]
	ds_read_b128 v[220:223], v13 offset:2048
	v_mfma_f32_16x16x32_bf16 v[88:91], v[180:183], v[168:171], v[88:91]
	ds_read_b128 v[224:227], v13 offset:4096
	v_mfma_f32_16x16x32_bf16 v[92:95], v[180:183], v[172:175], v[92:95]
	ds_read_b128 v[228:231], v13 offset:6144
	v_mfma_f32_16x16x32_bf16 v[96:99], v[184:187], v[160:163], v[96:99]
	ds_read_b128 v[232:235], v13 offset:8192
	v_mfma_f32_16x16x32_bf16 v[100:103], v[184:187], v[164:167], v[100:103]
	ds_read_b128 v[236:239], v13 offset:10240
	v_mfma_f32_16x16x32_bf16 v[104:107], v[184:187], v[168:171], v[104:107]
	v_mfma_f32_16x16x32_bf16 v[108:111], v[184:187], v[172:175], v[108:111]
	v_mfma_f32_16x16x32_bf16 v[112:115], v[188:191], v[160:163], v[112:115]
	v_mfma_f32_16x16x32_bf16 v[116:119], v[188:191], v[164:167], v[116:119]
	v_mfma_f32_16x16x32_bf16 v[120:123], v[188:191], v[168:171], v[120:123]
	v_mfma_f32_16x16x32_bf16 v[124:127], v[188:191], v[172:175], v[124:127]
	v_mfma_f32_16x16x32_bf16 v[128:131], v[192:195], v[160:163], v[128:131]
	v_mfma_f32_16x16x32_bf16 v[132:135], v[192:195], v[164:167], v[132:135]
	v_mfma_f32_16x16x32_bf16 v[136:139], v[192:195], v[168:171], v[136:139]
	v_mfma_f32_16x16x32_bf16 v[140:143], v[192:195], v[172:175], v[140:143]
	v_mfma_f32_16x16x32_bf16 v[144:147], v[196:199], v[160:163], v[144:147]
	v_mfma_f32_16x16x32_bf16 v[148:151], v[196:199], v[164:167], v[148:151]
	v_mfma_f32_16x16x32_bf16 v[152:155], v[196:199], v[168:171], v[152:155]
	v_mfma_f32_16x16x32_bf16 v[156:159], v[196:199], v[172:175], v[156:159]
	s_waitcnt lgkmcnt(0)
	v_mfma_f32_16x16x32_bf16 v[64:67], v[216:219], v[200:203], v[64:67]
	v_mfma_f32_16x16x32_bf16 v[68:71], v[216:219], v[204:207], v[68:71]
	global_load_dwordx4 v[160:163], v57, s[8:9] offset:128
	v_mfma_f32_16x16x32_bf16 v[72:75], v[216:219], v[208:211], v[72:75]
	v_mfma_f32_16x16x32_bf16 v[76:79], v[216:219], v[212:215], v[76:79]
	global_load_dwordx4 v[164:167], v57, s[8:9] offset:192
	v_mfma_f32_16x16x32_bf16 v[80:83], v[220:223], v[200:203], v[80:83]
	v_mfma_f32_16x16x32_bf16 v[84:87], v[220:223], v[204:207], v[84:87]
	global_load_dwordx4 v[168:171], v57, s[8:9] offset:256
	v_mfma_f32_16x16x32_bf16 v[88:91], v[220:223], v[208:211], v[88:91]
	v_mfma_f32_16x16x32_bf16 v[92:95], v[220:223], v[212:215], v[92:95]
	global_load_dwordx4 v[172:175], v57, s[8:9] offset:320
	v_mfma_f32_16x16x32_bf16 v[96:99], v[224:227], v[200:203], v[96:99]
	v_mfma_f32_16x16x32_bf16 v[100:103], v[224:227], v[204:207], v[100:103]
	global_load_dwordx4 v[176:179], v58, s[8:9] offset:0
	v_mfma_f32_16x16x32_bf16 v[104:107], v[224:227], v[208:211], v[104:107]
	v_mfma_f32_16x16x32_bf16 v[108:111], v[224:227], v[212:215], v[108:111]
	global_load_dwordx4 v[180:183], v58, s[8:9] offset:64
	v_mfma_f32_16x16x32_bf16 v[112:115], v[228:231], v[200:203], v[112:115]
	v_mfma_f32_16x16x32_bf16 v[116:119], v[228:231], v[204:207], v[116:119]
	global_load_dwordx4 v[184:187], v58, s[8:9] offset:128
	v_mfma_f32_16x16x32_bf16 v[120:123], v[228:231], v[208:211], v[120:123]
	v_mfma_f32_16x16x32_bf16 v[124:127], v[228:231], v[212:215], v[124:127]
	global_load_dwordx4 v[188:191], v58, s[8:9] offset:192
	v_mfma_f32_16x16x32_bf16 v[128:131], v[232:235], v[200:203], v[128:131]
	v_mfma_f32_16x16x32_bf16 v[132:135], v[232:235], v[204:207], v[132:135]
	global_load_dwordx4 v[192:195], v58, s[8:9] offset:256
	v_mfma_f32_16x16x32_bf16 v[136:139], v[232:235], v[208:211], v[136:139]
	v_mfma_f32_16x16x32_bf16 v[140:143], v[232:235], v[212:215], v[140:143]
	global_load_dwordx4 v[196:199], v58, s[8:9] offset:320
	v_mfma_f32_16x16x32_bf16 v[144:147], v[236:239], v[200:203], v[144:147]
	v_mfma_f32_16x16x32_bf16 v[148:151], v[236:239], v[204:207], v[148:151]
	v_mfma_f32_16x16x32_bf16 v[152:155], v[236:239], v[208:211], v[152:155]
	v_mfma_f32_16x16x32_bf16 v[156:159], v[236:239], v[212:215], v[156:159]
	v_and_b32_e32 v12, 63, v0
	v_cmp_gt_u32_e32 vcc, 16, v12
	v_xor_b32_e32 v13, 16, v12
	v_lshlrev_b32_e32 v13, 2, v13
	v_xor_b32_e32 v12, 32, v12
	v_lshlrev_b32_e32 v12, 2, v12
	v_bfe_u32 v14, v0, 6, 1
	v_mul_u32_u24_e32 v14, 0x60, v14
	v_bfe_u32 v15, v0, 4, 2
	v_lshl_add_u32 v14, v15, 2, v14
	v_add_u32_e32 v14, s13, v14
	v_lshlrev_b32_e32 v14, 2, v14
	global_load_dwordx4 v[200:203], v59, s[8:9] offset:0
	global_load_dwordx4 v[204:207], v59, s[8:9] offset:64
	global_load_dwordx4 v[208:211], v59, s[8:9] offset:128
	global_load_dwordx4 v[212:215], v59, s[8:9] offset:192
	global_load_dwordx4 v[216:219], v59, s[8:9] offset:256
	global_load_dwordx4 v[220:223], v59, s[8:9] offset:320
	v_lshrrev_b32_e32 v60, 1, v56
	v_lshrrev_b32_e32 v61, 1, v57
	v_lshrrev_b32_e32 v62, 1, v58
	v_lshrrev_b32_e32 v63, 1, v59
	v_bfe_u32 v2, v0, 4, 1
	v_mul_u32_u24_e32 v2, 24, v2
	v_add_u32_e32 v60, v60, v2
	v_add_u32_e32 v61, v61, v2
	v_add_u32_e32 v62, v62, v2
	v_add_u32_e32 v63, v63, v2
	v_bfe_u32 v8, v0, 7, 1
	v_and_b32_e32 v9, 15, v0
	v_lshl_add_u32 v8, v8, 6, v9
	v_add_u32_e32 v8, s12, v8
	v_lshlrev_b32_e32 v8, 6, v8
	v_bfe_u32 v9, v0, 6, 1
	v_lshlrev_b32_e32 v9, 1, v9
	v_add_u32_e32 v9, s30, v9
	v_lshl_add_u32 v8, v9, 2, v8
	v_add_u32_e32 v9, 0x400, v8
	v_add_u32_e32 v10, 0x400, v9
	v_add_u32_e32 v11, 0x400, v10
	s_waitcnt vmcnt(23)
	v_pk_add_f32 v[64:65], v[64:65], v[16:17]
	v_pk_add_f32 v[66:67], v[66:67], v[18:19]
	global_store_dwordx4 v56, v[64:67], s[10:11]
	v_pk_mul_f32 v[224:225], v[240:241], v[64:65]
	v_pk_mul_f32 v[226:227], v[242:243], v[66:67]
	v_cvt_pk_bf16_f32 v4, v224, v225
	v_cvt_pk_bf16_f32 v5, v226, v227
	v_pk_mul_f32 v[230:231], v[64:65], v[64:65]
	v_pk_mul_f32 v[232:233], v[66:67], v[66:67]
	v_add_f32_e32 v230, v230, v231
	v_add_f32_e32 v230, v232, v230
	v_add_f32_e32 v234, v233, v230
	s_waitcnt vmcnt(23)
	v_pk_add_f32 v[80:81], v[80:81], v[20:21]
	v_pk_add_f32 v[82:83], v[82:83], v[22:23]
	global_store_dwordx4 v56, v[80:83], s[10:11] offset:64
	v_pk_mul_f32 v[224:225], v[244:245], v[80:81]
	v_pk_mul_f32 v[226:227], v[246:247], v[82:83]
	v_cvt_pk_bf16_f32 v6, v224, v225
	v_cvt_pk_bf16_f32 v7, v226, v227
	s_nop 1
	v_permlane16_swap_b32 v4, v6
	v_permlane16_swap_b32 v5, v7
	global_store_dwordx4 v60, v[4:7], s[28:29]
	v_pk_mul_f32 v[230:231], v[80:81], v[80:81]
	v_pk_mul_f32 v[232:233], v[82:83], v[82:83]
	v_add_f32_e32 v230, v230, v231
	v_add_f32_e32 v230, v232, v230
	v_add_f32_e32 v230, v233, v230
	v_add_f32_e32 v234, v234, v230
	s_waitcnt vmcnt(24)
	v_pk_add_f32 v[96:97], v[96:97], v[24:25]
	v_pk_add_f32 v[98:99], v[98:99], v[26:27]
	global_store_dwordx4 v56, v[96:99], s[10:11] offset:128
	v_pk_mul_f32 v[224:225], v[248:249], v[96:97]
	v_pk_mul_f32 v[226:227], v[250:251], v[98:99]
	v_cvt_pk_bf16_f32 v4, v224, v225
	v_cvt_pk_bf16_f32 v5, v226, v227
	v_pk_mul_f32 v[230:231], v[96:97], v[96:97]
	v_pk_mul_f32 v[232:233], v[98:99], v[98:99]
	v_add_f32_e32 v230, v230, v231
	v_add_f32_e32 v230, v232, v230
	v_add_f32_e32 v230, v233, v230
	v_add_f32_e32 v234, v234, v230
	s_waitcnt vmcnt(24)
	v_pk_add_f32 v[112:113], v[112:113], v[28:29]
	v_pk_add_f32 v[114:115], v[114:115], v[30:31]
	global_store_dwordx4 v56, v[112:115], s[10:11] offset:192
	v_pk_mul_f32 v[224:225], v[252:253], v[112:113]
	v_pk_mul_f32 v[226:227], v[254:255], v[114:115]
	v_cvt_pk_bf16_f32 v6, v224, v225
	v_cvt_pk_bf16_f32 v7, v226, v227
	s_nop 1
	v_permlane16_swap_b32 v4, v6
	v_permlane16_swap_b32 v5, v7
	global_store_dwordx4 v60, v[4:7], s[28:29] offset:64
	v_pk_mul_f32 v[230:231], v[112:113], v[112:113]
	v_pk_mul_f32 v[232:233], v[114:115], v[114:115]
	v_add_f32_e32 v230, v230, v231
	v_add_f32_e32 v230, v232, v230
	v_add_f32_e32 v235, v233, v230
	s_waitcnt vmcnt(25)
	v_pk_add_f32 v[128:129], v[128:129], v[32:33]
	v_pk_add_f32 v[130:131], v[130:131], v[34:35]
	global_store_dwordx4 v56, v[128:131], s[10:11] offset:256
	v_pk_mul_f32 v[224:225], v[48:49], v[128:129]
	v_pk_mul_f32 v[226:227], v[50:51], v[130:131]
	v_cvt_pk_bf16_f32 v4, v224, v225
	v_cvt_pk_bf16_f32 v5, v226, v227
	v_pk_mul_f32 v[230:231], v[128:129], v[128:129]
	v_pk_mul_f32 v[232:233], v[130:131], v[130:131]
	v_add_f32_e32 v230, v230, v231
	v_add_f32_e32 v230, v232, v230
	v_add_f32_e32 v230, v233, v230
	v_add_f32_e32 v235, v235, v230
	s_waitcnt vmcnt(25)
	v_pk_add_f32 v[144:145], v[144:145], v[36:37]
	v_pk_add_f32 v[146:147], v[146:147], v[38:39]
	global_store_dwordx4 v56, v[144:147], s[10:11] offset:320
	v_pk_mul_f32 v[224:225], v[52:53], v[144:145]
	v_pk_mul_f32 v[226:227], v[54:55], v[146:147]
	v_cvt_pk_bf16_f32 v6, v224, v225
	v_cvt_pk_bf16_f32 v7, v226, v227
	s_nop 1
	v_permlane16_swap_b32 v4, v6
	v_permlane16_swap_b32 v5, v7
	global_store_dwordx4 v60, v[4:7], s[28:29] offset:128
	v_pk_mul_f32 v[230:231], v[144:145], v[144:145]
	v_pk_mul_f32 v[232:233], v[146:147], v[146:147]
	v_add_f32_e32 v230, v230, v231
	v_add_f32_e32 v230, v232, v230
	v_add_f32_e32 v230, v233, v230
	v_add_f32_e32 v235, v235, v230
	s_waitcnt vmcnt(26)
	v_pk_add_f32 v[68:69], v[68:69], v[40:41]
	v_pk_add_f32 v[70:71], v[70:71], v[42:43]
	global_store_dwordx4 v57, v[68:71], s[10:11]
	v_pk_mul_f32 v[224:225], v[240:241], v[68:69]
	v_pk_mul_f32 v[226:227], v[242:243], v[70:71]
	v_cvt_pk_bf16_f32 v4, v224, v225
	v_cvt_pk_bf16_f32 v5, v226, v227
	v_pk_mul_f32 v[230:231], v[68:69], v[68:69]
	v_pk_mul_f32 v[232:233], v[70:71], v[70:71]
	v_add_f32_e32 v230, v230, v231
	v_add_f32_e32 v230, v232, v230
	v_add_f32_e32 v236, v233, v230
	s_waitcnt vmcnt(26)
	v_pk_add_f32 v[84:85], v[84:85], v[44:45]
	v_pk_add_f32 v[86:87], v[86:87], v[46:47]
	global_store_dwordx4 v57, v[84:87], s[10:11] offset:64
	v_pk_mul_f32 v[224:225], v[244:245], v[84:85]
	v_pk_mul_f32 v[226:227], v[246:247], v[86:87]
	v_cvt_pk_bf16_f32 v6, v224, v225
	v_cvt_pk_bf16_f32 v7, v226, v227
	s_nop 1
	v_permlane16_swap_b32 v4, v6
	v_permlane16_swap_b32 v5, v7
	global_store_dwordx4 v61, v[4:7], s[28:29]
	v_pk_mul_f32 v[230:231], v[84:85], v[84:85]
	v_pk_mul_f32 v[232:233], v[86:87], v[86:87]
	v_add_f32_e32 v230, v230, v231
	v_add_f32_e32 v230, v232, v230
	v_add_f32_e32 v230, v233, v230
	v_add_f32_e32 v236, v236, v230
	s_waitcnt vmcnt(27)
	v_pk_add_f32 v[100:101], v[100:101], v[160:161]
	v_pk_add_f32 v[102:103], v[102:103], v[162:163]
	global_store_dwordx4 v57, v[100:103], s[10:11] offset:128
	v_pk_mul_f32 v[224:225], v[248:249], v[100:101]
	v_pk_mul_f32 v[226:227], v[250:251], v[102:103]
	v_cvt_pk_bf16_f32 v4, v224, v225
	v_cvt_pk_bf16_f32 v5, v226, v227
	v_pk_mul_f32 v[230:231], v[100:101], v[100:101]
	v_pk_mul_f32 v[232:233], v[102:103], v[102:103]
	v_add_f32_e32 v230, v230, v231
	v_add_f32_e32 v230, v232, v230
	v_add_f32_e32 v230, v233, v230
	v_add_f32_e32 v236, v236, v230
	s_waitcnt vmcnt(27)
	v_pk_add_f32 v[116:117], v[116:117], v[164:165]
	v_pk_add_f32 v[118:119], v[118:119], v[166:167]
	global_store_dwordx4 v57, v[116:119], s[10:11] offset:192
	v_pk_mul_f32 v[224:225], v[252:253], v[116:117]
	v_pk_mul_f32 v[226:227], v[254:255], v[118:119]
	v_cvt_pk_bf16_f32 v6, v224, v225
	v_cvt_pk_bf16_f32 v7, v226, v227
	s_nop 1
	v_permlane16_swap_b32 v4, v6
	v_permlane16_swap_b32 v5, v7
	global_store_dwordx4 v61, v[4:7], s[28:29] offset:64
	v_pk_mul_f32 v[230:231], v[116:117], v[116:117]
	v_pk_mul_f32 v[232:233], v[118:119], v[118:119]
	v_add_f32_e32 v230, v230, v231
	v_add_f32_e32 v230, v232, v230
	v_add_f32_e32 v237, v233, v230
	s_waitcnt vmcnt(28)
	v_pk_add_f32 v[132:133], v[132:133], v[168:169]
	v_pk_add_f32 v[134:135], v[134:135], v[170:171]
	global_store_dwordx4 v57, v[132:135], s[10:11] offset:256
	v_pk_mul_f32 v[224:225], v[48:49], v[132:133]
	v_pk_mul_f32 v[226:227], v[50:51], v[134:135]
	v_cvt_pk_bf16_f32 v4, v224, v225
	v_cvt_pk_bf16_f32 v5, v226, v227
	v_pk_mul_f32 v[230:231], v[132:133], v[132:133]
	v_pk_mul_f32 v[232:233], v[134:135], v[134:135]
	v_add_f32_e32 v230, v230, v231
	v_add_f32_e32 v230, v232, v230
	v_add_f32_e32 v230, v233, v230
	v_add_f32_e32 v237, v237, v230
	s_waitcnt vmcnt(28)
	v_pk_add_f32 v[148:149], v[148:149], v[172:173]
	v_pk_add_f32 v[150:151], v[150:151], v[174:175]
	global_store_dwordx4 v57, v[148:151], s[10:11] offset:320
	v_pk_mul_f32 v[224:225], v[52:53], v[148:149]
	v_pk_mul_f32 v[226:227], v[54:55], v[150:151]
	v_cvt_pk_bf16_f32 v6, v224, v225
	v_cvt_pk_bf16_f32 v7, v226, v227
	s_nop 1
	v_permlane16_swap_b32 v4, v6
	v_permlane16_swap_b32 v5, v7
	global_store_dwordx4 v61, v[4:7], s[28:29] offset:128
	v_pk_mul_f32 v[230:231], v[148:149], v[148:149]
	v_pk_mul_f32 v[232:233], v[150:151], v[150:151]
	v_add_f32_e32 v230, v230, v231
	v_add_f32_e32 v230, v232, v230
	v_add_f32_e32 v230, v233, v230
	v_add_f32_e32 v237, v237, v230
	s_waitcnt vmcnt(29)
	v_pk_add_f32 v[72:73], v[72:73], v[176:177]
	v_pk_add_f32 v[74:75], v[74:75], v[178:179]
	global_store_dwordx4 v58, v[72:75], s[10:11]
	v_pk_mul_f32 v[224:225], v[240:241], v[72:73]
	v_pk_mul_f32 v[226:227], v[242:243], v[74:75]
	v_cvt_pk_bf16_f32 v4, v224, v225
	v_cvt_pk_bf16_f32 v5, v226, v227
	v_pk_mul_f32 v[230:231], v[72:73], v[72:73]
	v_pk_mul_f32 v[232:233], v[74:75], v[74:75]
	v_add_f32_e32 v230, v230, v231
	v_add_f32_e32 v230, v232, v230
	v_add_f32_e32 v238, v233, v230
	s_waitcnt vmcnt(29)
	v_pk_add_f32 v[88:89], v[88:89], v[180:181]
	v_pk_add_f32 v[90:91], v[90:91], v[182:183]
	global_store_dwordx4 v58, v[88:91], s[10:11] offset:64
	v_pk_mul_f32 v[224:225], v[244:245], v[88:89]
	v_pk_mul_f32 v[226:227], v[246:247], v[90:91]
	v_cvt_pk_bf16_f32 v6, v224, v225
	v_cvt_pk_bf16_f32 v7, v226, v227
	s_nop 1
	v_permlane16_swap_b32 v4, v6
	v_permlane16_swap_b32 v5, v7
	global_store_dwordx4 v62, v[4:7], s[28:29]
	v_pk_mul_f32 v[230:231], v[88:89], v[88:89]
	v_pk_mul_f32 v[232:233], v[90:91], v[90:91]
	v_add_f32_e32 v230, v230, v231
	v_add_f32_e32 v230, v232, v230
	v_add_f32_e32 v230, v233, v230
	v_add_f32_e32 v238, v238, v230
	s_waitcnt vmcnt(30)
	v_pk_add_f32 v[104:105], v[104:105], v[184:185]
	v_pk_add_f32 v[106:107], v[106:107], v[186:187]
	global_store_dwordx4 v58, v[104:107], s[10:11] offset:128
	v_pk_mul_f32 v[224:225], v[248:249], v[104:105]
	v_pk_mul_f32 v[226:227], v[250:251], v[106:107]
	v_cvt_pk_bf16_f32 v4, v224, v225
	v_cvt_pk_bf16_f32 v5, v226, v227
	v_pk_mul_f32 v[230:231], v[104:105], v[104:105]
	v_pk_mul_f32 v[232:233], v[106:107], v[106:107]
	v_add_f32_e32 v230, v230, v231
	v_add_f32_e32 v230, v232, v230
	v_add_f32_e32 v230, v233, v230
	v_add_f32_e32 v238, v238, v230
	s_waitcnt vmcnt(30)
	v_pk_add_f32 v[120:121], v[120:121], v[188:189]
	v_pk_add_f32 v[122:123], v[122:123], v[190:191]
	global_store_dwordx4 v58, v[120:123], s[10:11] offset:192
	v_pk_mul_f32 v[224:225], v[252:253], v[120:121]
	v_pk_mul_f32 v[226:227], v[254:255], v[122:123]
	v_cvt_pk_bf16_f32 v6, v224, v225
	v_cvt_pk_bf16_f32 v7, v226, v227
	s_nop 1
	v_permlane16_swap_b32 v4, v6
	v_permlane16_swap_b32 v5, v7
	global_store_dwordx4 v62, v[4:7], s[28:29] offset:64
	v_pk_mul_f32 v[230:231], v[120:121], v[120:121]
	v_pk_mul_f32 v[232:233], v[122:123], v[122:123]
	v_add_f32_e32 v230, v230, v231
	v_add_f32_e32 v230, v232, v230
	v_add_f32_e32 v239, v233, v230
	s_waitcnt vmcnt(31)
	v_pk_add_f32 v[136:137], v[136:137], v[192:193]
	v_pk_add_f32 v[138:139], v[138:139], v[194:195]
	global_store_dwordx4 v58, v[136:139], s[10:11] offset:256
	v_pk_mul_f32 v[224:225], v[48:49], v[136:137]
	v_pk_mul_f32 v[226:227], v[50:51], v[138:139]
	v_cvt_pk_bf16_f32 v4, v224, v225
	v_cvt_pk_bf16_f32 v5, v226, v227
	v_pk_mul_f32 v[230:231], v[136:137], v[136:137]
	v_pk_mul_f32 v[232:233], v[138:139], v[138:139]
	v_add_f32_e32 v230, v230, v231
	v_add_f32_e32 v230, v232, v230
	v_add_f32_e32 v230, v233, v230
	v_add_f32_e32 v239, v239, v230
	s_waitcnt vmcnt(31)
	v_pk_add_f32 v[152:153], v[152:153], v[196:197]
	v_pk_add_f32 v[154:155], v[154:155], v[198:199]
	global_store_dwordx4 v58, v[152:155], s[10:11] offset:320
	v_pk_mul_f32 v[224:225], v[52:53], v[152:153]
	v_pk_mul_f32 v[226:227], v[54:55], v[154:155]
	v_cvt_pk_bf16_f32 v6, v224, v225
	v_cvt_pk_bf16_f32 v7, v226, v227
	s_nop 1
	v_permlane16_swap_b32 v4, v6
	v_permlane16_swap_b32 v5, v7
	global_store_dwordx4 v62, v[4:7], s[28:29] offset:128
	v_pk_mul_f32 v[230:231], v[152:153], v[152:153]
	v_pk_mul_f32 v[232:233], v[154:155], v[154:155]
	v_add_f32_e32 v230, v230, v231
	v_add_f32_e32 v230, v232, v230
	v_add_f32_e32 v230, v233, v230
	v_add_f32_e32 v239, v239, v230
	s_waitcnt vmcnt(32)
	v_pk_add_f32 v[76:77], v[76:77], v[200:201]
	v_pk_add_f32 v[78:79], v[78:79], v[202:203]
	global_store_dwordx4 v59, v[76:79], s[10:11]
	v_pk_mul_f32 v[224:225], v[240:241], v[76:77]
	v_pk_mul_f32 v[226:227], v[242:243], v[78:79]
	v_cvt_pk_bf16_f32 v4, v224, v225
	v_cvt_pk_bf16_f32 v5, v226, v227
	v_pk_mul_f32 v[230:231], v[76:77], v[76:77]
	v_pk_mul_f32 v[232:233], v[78:79], v[78:79]
	v_add_f32_e32 v230, v230, v231
	v_add_f32_e32 v230, v232, v230
	v_add_f32_e32 v14, v233, v230
	s_waitcnt vmcnt(32)
	v_pk_add_f32 v[92:93], v[92:93], v[204:205]
	v_pk_add_f32 v[94:95], v[94:95], v[206:207]
	global_store_dwordx4 v59, v[92:95], s[10:11] offset:64
	v_pk_mul_f32 v[224:225], v[244:245], v[92:93]
	v_pk_mul_f32 v[226:227], v[246:247], v[94:95]
	v_cvt_pk_bf16_f32 v6, v224, v225
	v_cvt_pk_bf16_f32 v7, v226, v227
	s_nop 1
	v_permlane16_swap_b32 v4, v6
	v_permlane16_swap_b32 v5, v7
	global_store_dwordx4 v63, v[4:7], s[28:29]
	v_pk_mul_f32 v[230:231], v[92:93], v[92:93]
	v_pk_mul_f32 v[232:233], v[94:95], v[94:95]
	v_add_f32_e32 v230, v230, v231
	v_add_f32_e32 v230, v232, v230
	v_add_f32_e32 v230, v233, v230
	v_add_f32_e32 v14, v14, v230
	s_waitcnt vmcnt(33)
	v_pk_add_f32 v[108:109], v[108:109], v[208:209]
	v_pk_add_f32 v[110:111], v[110:111], v[210:211]
	global_store_dwordx4 v59, v[108:111], s[10:11] offset:128
	v_pk_mul_f32 v[224:225], v[248:249], v[108:109]
	v_pk_mul_f32 v[226:227], v[250:251], v[110:111]
	v_cvt_pk_bf16_f32 v4, v224, v225
	v_cvt_pk_bf16_f32 v5, v226, v227
	v_pk_mul_f32 v[230:231], v[108:109], v[108:109]
	v_pk_mul_f32 v[232:233], v[110:111], v[110:111]
	v_add_f32_e32 v230, v230, v231
	v_add_f32_e32 v230, v232, v230
	v_add_f32_e32 v230, v233, v230
	v_add_f32_e32 v14, v14, v230
	s_waitcnt vmcnt(33)
	v_pk_add_f32 v[124:125], v[124:125], v[212:213]
	v_pk_add_f32 v[126:127], v[126:127], v[214:215]
	global_store_dwordx4 v59, v[124:127], s[10:11] offset:192
	v_pk_mul_f32 v[224:225], v[252:253], v[124:125]
	v_pk_mul_f32 v[226:227], v[254:255], v[126:127]
	v_cvt_pk_bf16_f32 v6, v224, v225
	v_cvt_pk_bf16_f32 v7, v226, v227
	s_nop 1
	v_permlane16_swap_b32 v4, v6
	v_permlane16_swap_b32 v5, v7
	global_store_dwordx4 v63, v[4:7], s[28:29] offset:64
	v_pk_mul_f32 v[230:231], v[124:125], v[124:125]
	v_pk_mul_f32 v[232:233], v[126:127], v[126:127]
	v_add_f32_e32 v230, v230, v231
	v_add_f32_e32 v230, v232, v230
	v_add_f32_e32 v15, v233, v230
	s_waitcnt vmcnt(34)
	v_pk_add_f32 v[140:141], v[140:141], v[216:217]
	v_pk_add_f32 v[142:143], v[142:143], v[218:219]
	global_store_dwordx4 v59, v[140:143], s[10:11] offset:256
	v_pk_mul_f32 v[224:225], v[48:49], v[140:141]
	v_pk_mul_f32 v[226:227], v[50:51], v[142:143]
	v_cvt_pk_bf16_f32 v4, v224, v225
	v_cvt_pk_bf16_f32 v5, v226, v227
	v_pk_mul_f32 v[230:231], v[140:141], v[140:141]
	v_pk_mul_f32 v[232:233], v[142:143], v[142:143]
	v_add_f32_e32 v230, v230, v231
	v_add_f32_e32 v230, v232, v230
	v_add_f32_e32 v230, v233, v230
	v_add_f32_e32 v15, v15, v230
	s_waitcnt vmcnt(34)
	v_pk_add_f32 v[156:157], v[156:157], v[220:221]
	v_pk_add_f32 v[158:159], v[158:159], v[222:223]
	global_store_dwordx4 v59, v[156:159], s[10:11] offset:320
	v_pk_mul_f32 v[224:225], v[52:53], v[156:157]
	v_pk_mul_f32 v[226:227], v[54:55], v[158:159]
	v_cvt_pk_bf16_f32 v6, v224, v225
	v_cvt_pk_bf16_f32 v7, v226, v227
	s_nop 1
	v_permlane16_swap_b32 v4, v6
	v_permlane16_swap_b32 v5, v7
	global_store_dwordx4 v63, v[4:7], s[28:29] offset:128
	v_pk_mul_f32 v[230:231], v[156:157], v[156:157]
	v_pk_mul_f32 v[232:233], v[158:159], v[158:159]
	v_add_f32_e32 v230, v230, v231
	v_add_f32_e32 v230, v232, v230
	v_add_f32_e32 v230, v233, v230
	v_add_f32_e32 v15, v15, v230
	ds_bpermute_b32 v224, v13, v234
	ds_bpermute_b32 v225, v13, v235
	ds_bpermute_b32 v226, v13, v236
	ds_bpermute_b32 v227, v13, v237
	ds_bpermute_b32 v228, v13, v238
	ds_bpermute_b32 v229, v13, v239
	ds_bpermute_b32 v230, v13, v14
	ds_bpermute_b32 v231, v13, v15
	s_waitcnt lgkmcnt(0)
	v_add_f32_e32 v234, v234, v224
	v_add_f32_e32 v235, v235, v225
	v_add_f32_e32 v236, v236, v226
	v_add_f32_e32 v237, v237, v227
	v_add_f32_e32 v238, v238, v228
	v_add_f32_e32 v239, v239, v229
	v_add_f32_e32 v14, v14, v230
	v_add_f32_e32 v15, v15, v231
	ds_bpermute_b32 v224, v12, v234
	ds_bpermute_b32 v225, v12, v235
	ds_bpermute_b32 v226, v12, v236
	ds_bpermute_b32 v227, v12, v237
	ds_bpermute_b32 v228, v12, v238
	ds_bpermute_b32 v229, v12, v239
	ds_bpermute_b32 v230, v12, v14
	ds_bpermute_b32 v231, v12, v15
	s_waitcnt lgkmcnt(0)
	v_add_f32_e32 v234, v234, v224
	v_add_f32_e32 v235, v235, v225
	v_add_f32_e32 v236, v236, v226
	v_add_f32_e32 v237, v237, v227
	v_add_f32_e32 v238, v238, v228
	v_add_f32_e32 v239, v239, v229
	v_add_f32_e32 v14, v14, v230
	v_add_f32_e32 v15, v15, v231
	s_and_saveexec_b64 s[2:3], vcc
	global_store_dwordx2 v8, v[234:235], s[26:27]
	global_store_dwordx2 v9, v[236:237], s[26:27]
	global_store_dwordx2 v10, v[238:239], s[26:27]
	global_store_dwordx2 v11, v[14:15], s[26:27]
	s_or_b64 exec, exec, s[2:3]
